# E37: E36 + adaLN prologue loop requests the next 8 weight rows one iteration ahead (second register set), no per-row vmcnt ladder
# speedup vs baseline: 1.0228x; 1.0060x over previous
.LBB0_22:
	s_or_b64 exec, exec, s[0:1]
	s_and_b32 s0, s50, 0xff
	s_add_i32 s1, 0, 0x22110
	s_mulk_i32 s0, 0xab
	v_mov_b32_e32 v1, s1
	s_lshr_b32 s8, s0, 13
	s_waitcnt lgkmcnt(0)
	s_barrier
	ds_read_b64 v[2:3], v1
	s_mul_i32 s0, s8, 48
	s_sub_i32 s0, s50, s0
	s_mul_i32 s9, s8, 0x1800000
	s_lshl_b32 s12, s29, 7
	s_mul_i32 s13, s29, 0x300000
	s_mul_hi_i32 s12, s12, 0x6000
	s_add_u32 s13, s9, s13
	s_addc_u32 s12, 0, s12
	s_and_b32 s9, s0, 0xff
	s_lshl_b32 s0, s9, 9
	s_waitcnt lgkmcnt(0)
	v_readfirstlane_b32 s11, v2
	s_or_b32 s0, s13, s0
	v_readfirstlane_b32 s1, v3
	s_add_u32 s0, s11, s0
	v_lshlrev_b32_e32 v4, 3, v34
	v_mov_b32_e32 v5, 0
	s_addc_u32 s1, s1, s12
	v_lshl_add_u64 v[2:3], s[0:1], 0, v[4:5]
	s_lshl_b32 s0, s29, 9
	s_movk_i32 s10, 0x6000
	s_add_i32 s11, s0, 0
	s_mov_b64 s[0:1], 0
	s_mov_b32 s12, 0xc000
	s_mov_b32 s13, 0x12000
	s_mov_b32 s14, 0x18000
	s_mov_b32 s15, 0x1e000
	s_mov_b32 s16, 0x24000
	s_mov_b32 s17, 0x2a000
	v_mov_b32_e32 v4, v5
	v_mov_b32_e32 v6, v5
	v_mov_b32_e32 v7, v5
	v_mov_b32_e32 v8, v5
	v_mov_b32_e32 v9, v5
	v_mov_b32_e32 v10, v5
	v_mov_b32_e32 v11, v5
	v_lshl_add_u64 v[12:13], v[2:3], 0, s[0:1]
	v_add_co_u32_e32 v14, vcc, s10, v12
	v_mov_b64_e32 v[96:97], v[12:13]
	s_nop 0
	v_addc_co_u32_e32 v15, vcc, 0, v13, vcc
	v_add_co_u32_e32 v16, vcc, s12, v12
	s_nop 0
	s_nop 0
	v_addc_co_u32_e32 v17, vcc, 0, v13, vcc
	v_add_co_u32_e32 v18, vcc, s13, v12
	s_nop 0
	s_nop 0
	v_addc_co_u32_e32 v19, vcc, 0, v13, vcc
	v_add_co_u32_e32 v20, vcc, s14, v12
	s_nop 0
	s_nop 0
	v_addc_co_u32_e32 v21, vcc, 0, v13, vcc
	v_add_co_u32_e32 v22, vcc, s15, v12
	s_nop 0
	s_nop 0
	v_addc_co_u32_e32 v23, vcc, 0, v13, vcc
	v_add_co_u32_e32 v24, vcc, s16, v12
	s_nop 0
	s_nop 0
	v_addc_co_u32_e32 v25, vcc, 0, v13, vcc
	v_add_co_u32_e32 v12, vcc, s17, v12
	s_nop 1
	v_addc_co_u32_e32 v13, vcc, 0, v13, vcc
	global_load_dwordx2 v[80:81], v[96:97], off nt
	global_load_dwordx2 v[82:83], v[14:15], off nt
	global_load_dwordx2 v[84:85], v[16:17], off nt
	global_load_dwordx2 v[86:87], v[18:19], off nt
	global_load_dwordx2 v[88:89], v[20:21], off nt
	global_load_dwordx2 v[90:91], v[22:23], off nt
	global_load_dwordx2 v[92:93], v[24:25], off nt
	global_load_dwordx2 v[94:95], v[12:13], off nt
.LBB0_23:
	s_waitcnt vmcnt(0)
	v_mov_b64_e32 v[32:33], v[80:81]
	v_mov_b64_e32 v[48:49], v[82:83]
	v_mov_b64_e32 v[50:51], v[84:85]
	v_mov_b64_e32 v[52:53], v[86:87]
	v_mov_b64_e32 v[54:55], v[88:89]
	v_mov_b64_e32 v[56:57], v[90:91]
	v_mov_b64_e32 v[58:59], v[92:93]
	v_mov_b64_e32 v[60:61], v[94:95]
	s_add_u32 s0, s0, 0x30000
	s_addc_u32 s1, s1, 0
	v_lshl_add_u64 v[12:13], v[2:3], 0, s[0:1]
	v_add_co_u32_e32 v14, vcc, s10, v12
	v_mov_b64_e32 v[96:97], v[12:13]
	s_nop 0
	v_addc_co_u32_e32 v15, vcc, 0, v13, vcc
	v_add_co_u32_e32 v16, vcc, s12, v12
	v_mov_b32_e32 v1, s11
	s_nop 0
	v_addc_co_u32_e32 v17, vcc, 0, v13, vcc
	v_add_co_u32_e32 v18, vcc, s13, v12
	s_nop 0
	s_nop 0
	v_addc_co_u32_e32 v19, vcc, 0, v13, vcc
	v_add_co_u32_e32 v20, vcc, s14, v12
	s_nop 0
	s_nop 0
	v_addc_co_u32_e32 v21, vcc, 0, v13, vcc
	v_add_co_u32_e32 v22, vcc, s15, v12
	s_add_i32 s11, s11, 32
	s_nop 0
	v_addc_co_u32_e32 v23, vcc, 0, v13, vcc
	v_add_co_u32_e32 v24, vcc, s16, v12
	s_cmp_eq_u32 s0, 0x300000
	s_nop 0
	v_addc_co_u32_e32 v25, vcc, 0, v13, vcc
	v_add_co_u32_e32 v12, vcc, s17, v12
	s_nop 1
	v_addc_co_u32_e32 v13, vcc, 0, v13, vcc
	s_cbranch_scc1 .Lada_skip
	global_load_dwordx2 v[80:81], v[96:97], off nt
	global_load_dwordx2 v[82:83], v[14:15], off nt
	global_load_dwordx2 v[84:85], v[16:17], off nt
	global_load_dwordx2 v[86:87], v[18:19], off nt
	global_load_dwordx2 v[88:89], v[20:21], off nt
	global_load_dwordx2 v[90:91], v[22:23], off nt
	global_load_dwordx2 v[92:93], v[24:25], off nt
	global_load_dwordx2 v[94:95], v[12:13], off nt
.Lada_skip:
	ds_read_b128 v[12:15], v1
	ds_read_b128 v[16:19], v1 offset:16
	ds_read_b128 v[20:23], v1 offset:4096
	ds_read_b128 v[24:27], v1 offset:4112
	ds_read_b128 v[28:31], v1 offset:8192
	ds_read_b128 v[36:39], v1 offset:8208
	ds_read_b128 v[40:43], v1 offset:12288
	ds_read_b128 v[44:47], v1 offset:12304
	s_waitcnt lgkmcnt(7)
	v_mov_b32_e32 v62, v15
	s_waitcnt lgkmcnt(5)
	v_mov_b32_e32 v64, v23
	s_waitcnt lgkmcnt(3)
	v_mov_b32_e32 v66, v31
	s_waitcnt lgkmcnt(1)
	v_mov_b32_e32 v68, v43
	v_mov_b32_e32 v70, v19
	v_mov_b32_e32 v72, v27
	v_mov_b32_e32 v74, v39
	s_waitcnt lgkmcnt(0)
	v_mov_b32_e32 v76, v47
	v_pk_fma_f32 v[6:7], v[32:33], v[12:13], v[6:7] op_sel_hi:[1,0,1]
	v_pk_fma_f32 v[8:9], v[32:33], v[20:21], v[8:9] op_sel_hi:[1,0,1]
	v_pk_fma_f32 v[10:11], v[32:33], v[28:29], v[10:11] op_sel_hi:[1,0,1]
	v_pk_fma_f32 v[4:5], v[32:33], v[40:41], v[4:5] op_sel_hi:[1,0,1]
	v_pk_fma_f32 v[6:7], v[48:49], v[12:13], v[6:7] op_sel:[0,1,0]
	v_pk_fma_f32 v[8:9], v[48:49], v[20:21], v[8:9] op_sel:[0,1,0]
	v_pk_fma_f32 v[10:11], v[48:49], v[28:29], v[10:11] op_sel:[0,1,0]
	v_pk_fma_f32 v[4:5], v[48:49], v[40:41], v[4:5] op_sel:[0,1,0]
	v_pk_fma_f32 v[6:7], v[50:51], v[14:15], v[6:7] op_sel_hi:[1,0,1]
	v_pk_fma_f32 v[8:9], v[50:51], v[22:23], v[8:9] op_sel_hi:[1,0,1]
	v_pk_fma_f32 v[10:11], v[50:51], v[30:31], v[10:11] op_sel_hi:[1,0,1]
	v_pk_fma_f32 v[4:5], v[50:51], v[42:43], v[4:5] op_sel_hi:[1,0,1]
	v_pk_fma_f32 v[6:7], v[52:53], v[62:63], v[6:7] op_sel_hi:[1,0,1]
	v_pk_fma_f32 v[8:9], v[52:53], v[64:65], v[8:9] op_sel_hi:[1,0,1]
	v_pk_fma_f32 v[10:11], v[52:53], v[66:67], v[10:11] op_sel_hi:[1,0,1]
	v_pk_fma_f32 v[4:5], v[52:53], v[68:69], v[4:5] op_sel_hi:[1,0,1]
	v_pk_fma_f32 v[6:7], v[54:55], v[16:17], v[6:7] op_sel_hi:[1,0,1]
	v_pk_fma_f32 v[8:9], v[54:55], v[24:25], v[8:9] op_sel_hi:[1,0,1]
	v_pk_fma_f32 v[10:11], v[54:55], v[36:37], v[10:11] op_sel_hi:[1,0,1]
	v_pk_fma_f32 v[4:5], v[54:55], v[44:45], v[4:5] op_sel_hi:[1,0,1]
	v_pk_fma_f32 v[6:7], v[56:57], v[16:17], v[6:7] op_sel:[0,1,0]
	v_pk_fma_f32 v[8:9], v[56:57], v[24:25], v[8:9] op_sel:[0,1,0]
	v_pk_fma_f32 v[10:11], v[56:57], v[36:37], v[10:11] op_sel:[0,1,0]
	v_pk_fma_f32 v[4:5], v[56:57], v[44:45], v[4:5] op_sel:[0,1,0]
	v_pk_fma_f32 v[6:7], v[58:59], v[18:19], v[6:7] op_sel_hi:[1,0,1]
	v_pk_fma_f32 v[8:9], v[58:59], v[26:27], v[8:9] op_sel_hi:[1,0,1]
	v_pk_fma_f32 v[10:11], v[58:59], v[38:39], v[10:11] op_sel_hi:[1,0,1]
	v_pk_fma_f32 v[4:5], v[58:59], v[46:47], v[4:5] op_sel_hi:[1,0,1]
	v_pk_fma_f32 v[6:7], v[60:61], v[70:71], v[6:7] op_sel_hi:[1,0,1]
	v_pk_fma_f32 v[8:9], v[60:61], v[72:73], v[8:9] op_sel_hi:[1,0,1]
	v_pk_fma_f32 v[10:11], v[60:61], v[74:75], v[10:11] op_sel_hi:[1,0,1]
	v_pk_fma_f32 v[4:5], v[60:61], v[76:77], v[4:5] op_sel_hi:[1,0,1]
	s_cbranch_scc0 .LBB0_23
	s_lshl_b32 s0, s29, 11
	s_add_i32 s0, s0, 0
	v_lshl_add_u32 v1, v34, 3, s0
	s_add_i32 s0, 0, 0x22118
	ds_write2st64_b64 v1, v[6:7], v[8:9] offset0:32 offset1:33
	ds_write2st64_b64 v1, v[10:11], v[4:5] offset0:34 offset1:35
	v_mov_b32_e32 v1, s0
	s_waitcnt lgkmcnt(0)
	s_barrier
	ds_read_b64 v[2:3], v1
	s_lshl_b32 s9, s9, 7
	s_mul_i32 s10, s8, 0x1800
	v_and_b32_e32 v1, 0x7f, v0
	s_add_i32 s10, s10, s9
	s_waitcnt lgkmcnt(0)
	v_readfirstlane_b32 s0, v2
	v_or_b32_e32 v2, s10, v1
	v_readfirstlane_b32 s1, v3
	v_lshlrev_b32_e32 v2, 2, v2
	v_lshrrev_b32_e32 v3, 7, v0
	v_lshlrev_b32_e32 v4, 2, v1
	v_lshl_add_u32 v3, s8, 2, v3
	s_nop 0
	global_load_dword v12, v2, s[0:1]
	v_and_b32_e32 v2, 0x3fffff80, v0
	v_lshlrev_b32_e32 v2, 2, v2
	s_movk_i32 s0, 0x1800
	v_add3_u32 v8, 0, v2, v4
	v_mul_lo_u32 v10, v3, s0
	ds_read2st64_b32 v[2:3], v8 offset0:64 offset1:72
	ds_read2st64_b32 v[4:5], v8 offset0:80 offset1:88
	ds_read2st64_b32 v[6:7], v8 offset0:96 offset1:104
	ds_read2st64_b32 v[8:9], v8 offset0:112 offset1:120
	v_add_u32_e32 v10, s9, v10
	v_or_b32_e32 v10, v10, v1
	v_ashrrev_i32_e32 v11, 31, v10
	v_lshl_add_u64 v[10:11], v[10:11], 2, s[2:3]
	v_add_co_u32_e32 v10, vcc, 0x100000, v10
	s_waitcnt vmcnt(0) lgkmcnt(3)
	v_add_f32_e32 v1, v12, v2
	v_add_f32_e32 v1, v1, v3
	s_waitcnt lgkmcnt(2)
	v_add_f32_e32 v1, v1, v4
	v_add_f32_e32 v1, v1, v5
	s_waitcnt lgkmcnt(1)
	v_add_f32_e32 v1, v1, v6
	v_add_f32_e32 v1, v1, v7
	s_waitcnt lgkmcnt(0)
	v_add_f32_e32 v1, v1, v8
	v_addc_co_u32_e32 v11, vcc, 0, v11, vcc
	v_add_f32_e32 v1, v1, v9
	global_store_dword v[10:11], v1, off
	s_barrier
